# mixer phases: 2 of every 8 workgroup rows (instead of 3) start on the expert-weight conversion queue, so the conversion stream takes less of the HBM bandwidth away from the compute units at the start
# speedup vs baseline: 1.0108x; 1.0108x over previous
.LBB0_553:
	s_cmp_lt_i32 s42, 4
	s_cselect_b64 s[4:5], -1, 0
	s_cmp_gt_i32 s43, 3
	s_cselect_b64 s[6:7], -1, 0
	s_and_b64 s[4:5], s[4:5], s[6:7]
	s_andn2_b64 vcc, exec, s[4:5]
	s_cbranch_vccnz .LBB0_862
	s_and_b32 s4, s2, 56
	s_cmp_gt_u32 s4, 15
	s_waitcnt lgkmcnt(0)
	s_cselect_b64 s[8:9], -1, 0
	s_and_b64 vcc, exec, s[8:9]
	v_mov_b32 v1, v0
	s_nop 0
	v_mov_b32 v1, v0
	s_nop 0
	v_mov_b32 v1, v0
	s_cbranch_vccnz .LBB0_569
	s_add_u32 s4, s40, 0x6800
	s_addc_u32 s5, s41, 0
	s_and_saveexec_b64 s[6:7], s[36:37]
	s_cbranch_execz .LBB0_559
	s_mov_b64 s[12:13], exec
	v_mbcnt_lo_u32_b32 v1, s12, 0
	v_mbcnt_hi_u32_b32 v1, s13, v1
	v_cmp_eq_u32_e32 vcc, 0, v1
	s_and_saveexec_b64 s[10:11], vcc
	s_cbranch_execz .LBB0_558
	s_bcnt1_i32_b64 s12, s[12:13]
	v_mov_b32_e32 v2, 0
	s_waitcnt vmcnt(0)
	v_mov_b32_e32 v3, s12
	global_atomic_add v2, v2, v3, s[4:5] sc0

.LBB0_922:
	s_cmp_lt_i32 s42, 6
	s_cselect_b64 s[4:5], -1, 0
	s_cmp_gt_i32 s43, 5
	s_cselect_b64 s[6:7], -1, 0
	s_and_b64 s[4:5], s[4:5], s[6:7]
	s_andn2_b64 vcc, exec, s[4:5]
	s_cbranch_vccnz .LBB0_1504
	s_and_b32 s4, s2, 56
	s_cmp_gt_u32 s4, 15
	s_cselect_b64 s[46:47], -1, 0
	s_and_b64 vcc, exec, s[46:47]
	v_mov_b32 v1, v0
	s_nop 0
	v_mov_b32 v1, v0
	s_nop 0
	v_mov_b32 v1, v0
	s_cbranch_vccnz .LBB0_943
	s_add_u32 s4, s40, 0x6900
	s_addc_u32 s5, s41, 0
	s_and_saveexec_b64 s[6:7], s[36:37]
	s_cbranch_execz .LBB0_928
	s_mov_b64 s[10:11], exec
	v_mbcnt_lo_u32_b32 v1, s10, 0
	v_mbcnt_hi_u32_b32 v1, s11, v1
	v_cmp_eq_u32_e32 vcc, 0, v1
	s_waitcnt lgkmcnt(0)
	s_and_saveexec_b64 s[8:9], vcc
	s_cbranch_execz .LBB0_927
	s_bcnt1_i32_b64 s10, s[10:11]
	v_mov_b32_e32 v2, 0
	s_waitcnt vmcnt(0)
	v_mov_b32_e32 v3, s10
	global_atomic_add v2, v2, v3, s[4:5] sc0

.LBB0_2279:
	s_cmp_lt_i32 s42, 14
	s_cselect_b64 s[4:5], -1, 0
	s_cmp_gt_i32 s43, 13
	s_cselect_b64 s[6:7], -1, 0
	s_and_b64 s[4:5], s[4:5], s[6:7]
	s_andn2_b64 vcc, exec, s[4:5]
	s_cbranch_vccnz .LBB0_2588
	s_and_b32 s4, s2, 56
	s_cmp_gt_u32 s4, 15
	s_waitcnt lgkmcnt(0)
	s_cselect_b64 s[8:9], -1, 0
	s_and_b64 vcc, exec, s[8:9]
	v_mov_b32 v1, v0
	s_nop 0
	v_mov_b32 v1, v0
	s_nop 0
	v_mov_b32 v1, v0
	s_cbranch_vccnz .LBB0_2295
	s_add_u32 s4, s40, 0x6a00
	s_addc_u32 s5, s41, 0
	s_and_saveexec_b64 s[6:7], s[36:37]
	s_cbranch_execz .LBB0_2285
	s_mov_b64 s[12:13], exec
	v_mbcnt_lo_u32_b32 v1, s12, 0
	v_mbcnt_hi_u32_b32 v1, s13, v1
	v_cmp_eq_u32_e32 vcc, 0, v1
	s_and_saveexec_b64 s[10:11], vcc
	s_cbranch_execz .LBB0_2284
	s_bcnt1_i32_b64 s12, s[12:13]
	v_mov_b32_e32 v2, 0
	s_waitcnt vmcnt(0)
	v_mov_b32_e32 v3, s12
	global_atomic_add v2, v2, v3, s[4:5] sc0

.LBB0_2648:
	s_cmp_lt_i32 s42, 16
	s_cselect_b64 s[4:5], -1, 0
	s_cmp_gt_i32 s43, 15
	s_cselect_b64 s[6:7], -1, 0
	s_and_b64 s[4:5], s[4:5], s[6:7]
	s_andn2_b64 vcc, exec, s[4:5]
	s_cbranch_vccnz .LBB0_3018
	s_and_b32 s4, s2, 56
	s_cmp_gt_u32 s4, 15
	s_cselect_b64 s[46:47], -1, 0
	s_and_b64 vcc, exec, s[46:47]
	v_mov_b32 v1, v0
	s_nop 0
	v_mov_b32 v1, v0
	s_nop 0
	v_mov_b32 v1, v0
	s_cbranch_vccnz .LBB0_2669
	s_add_u32 s4, s40, 0x6b00
	s_addc_u32 s5, s41, 0
	s_and_saveexec_b64 s[6:7], s[36:37]
	s_cbranch_execz .LBB0_2654
	s_mov_b64 s[10:11], exec
	v_mbcnt_lo_u32_b32 v1, s10, 0
	v_mbcnt_hi_u32_b32 v1, s11, v1
	v_cmp_eq_u32_e32 vcc, 0, v1
	s_waitcnt lgkmcnt(0)
	s_and_saveexec_b64 s[8:9], vcc
	s_cbranch_execz .LBB0_2653
	s_bcnt1_i32_b64 s10, s[10:11]
	v_mov_b32_e32 v2, 0
	s_waitcnt vmcnt(0)
	v_mov_b32_e32 v3, s10
	global_atomic_add v2, v2, v3, s[4:5] sc0
